# speedup vs baseline: 1.0283x; 1.0019x over previous
.LBB1_6:
	s_waitcnt lgkmcnt(14)
	v_mfma_f32_32x32x16_f16 v[34:49], v[162:165], v[122:125], v[34:49]
	v_exp_f32_e32 v98, v98
	v_exp_f32_e32 v99, v99
	v_exp_f32_e32 v100, v100
	v_exp_f32_e32 v101, v101
	s_sub_i32 s43, s38, s27
	s_add_i32 s43, s43, 34
	s_add_i32 s44, s18, -1
	s_cmp_ge_i32 s44, s28
	s_cselect_b32 s45, s28, 0
	s_sub_i32 s44, s44, s45
	s_and_b64 s[48:49], s[6:7], exec
	s_cselect_b32 s43, s44, s43
	v_mad_i64_i32 v[252:253], s[50:51], s43, v244, v[222:223]
	s_add_i32 s44, s38, 1
	s_cmp_ge_i32 s44, s29
	s_cselect_b32 s44, s29, 0
	s_sub_i32 s44, 0, s44
	s_and_b64 s[48:49], s[6:7], exec
	s_cselect_b32 s44, s44, s28
	s_add_i32 s44, s44, s18
	s_add_i32 s44, s44, -3
	v_mad_i64_i32 v[254:255], s[50:51], s44, v244, v[224:225]
	s_add_i32 s52, s35, s30
	s_add_i32 s53, s36, s31
	s_waitcnt lgkmcnt(12)
	v_mfma_f32_32x32x16_f16 v[18:33], v[162:165], v[118:121], v[18:33]
	v_exp_f32_e32 v102, v102
	v_exp_f32_e32 v103, v103
	v_exp_f32_e32 v104, v104
	v_exp_f32_e32 v105, v105
	v_add_u32_e32 v74, s36, v234
	ds_read_b128 v[62:65], v74
	ds_read_b128 v[138:141], v74 offset:4096
	s_waitcnt lgkmcnt(12)
	v_mfma_f32_32x32x16_f16 v[34:49], v[166:169], v[114:117], v[34:49]
	v_exp_f32_e32 v106, v106
	v_exp_f32_e32 v107, v107
	v_exp_f32_e32 v108, v108
	v_exp_f32_e32 v109, v109
	v_add_u32_e32 v74, s36, v235
	ds_read_b128 v[178:181], v74
	ds_read_b128 v[126:129], v74 offset:4096
	s_waitcnt lgkmcnt(12)
	v_mfma_f32_32x32x16_f16 v[18:33], v[166:169], v[70:73], v[18:33]
	v_exp_f32_e32 v110, v110
	v_exp_f32_e32 v111, v111
	v_exp_f32_e32 v112, v112
	v_exp_f32_e32 v113, v113
	v_add_u32_e32 v70, s36, v236
	ds_read_b128 v[130:133], v70
	ds_read_b128 v[118:121], v70 offset:4096
	s_waitcnt lgkmcnt(12)
	v_mfma_f32_32x32x16_f16 v[34:49], v[170:173], v[66:69], v[34:49]
	v_exp_f32_e32 v82, v82
	v_exp_f32_e32 v83, v83
	v_exp_f32_e32 v84, v84
	v_exp_f32_e32 v85, v85
	v_add_u32_e32 v66, s36, v237
	ds_read_b128 v[122:125], v66
	ds_read_b128 v[114:117], v66 offset:4096
	s_waitcnt lgkmcnt(12)
	v_mfma_f32_32x32x16_f16 v[18:33], v[170:173], v[50:53], v[18:33]
	v_exp_f32_e32 v86, v86
	v_exp_f32_e32 v87, v87
	v_exp_f32_e32 v88, v88
	v_exp_f32_e32 v89, v89
	s_waitcnt lgkmcnt(10)
	v_mfma_f32_32x32x16_f16 v[34:49], v[174:177], v[54:57], v[34:49]
	v_exp_f32_e32 v90, v90
	v_exp_f32_e32 v91, v91
	v_exp_f32_e32 v92, v92
	v_exp_f32_e32 v93, v93
	s_waitcnt lgkmcnt(8)
	v_mfma_f32_32x32x16_f16 v[18:33], v[174:177], v[58:61], v[18:33]
	v_exp_f32_e32 v94, v94
	v_exp_f32_e32 v95, v95
	v_exp_f32_e32 v96, v96
	v_exp_f32_e32 v97, v97
	s_mov_b32 m0, s52
	s_addk_i32 s52, 0x1000
	global_load_lds_dwordx4 v[252:253], off
	s_mov_b32 m0, s52
	v_lshl_add_u64 v[252:253], v[252:253], 0, s[10:11]
	global_load_lds_dwordx4 v[252:253], off
	s_mov_b32 m0, s53
	s_addk_i32 s53, 0x1000
	global_load_lds_dwordx4 v[254:255], off
	s_mov_b32 m0, s53
	v_lshl_add_u64 v[254:255], v[254:255], 0, s[10:11]
	global_load_lds_dwordx4 v[254:255], off
	s_waitcnt vmcnt(4) lgkmcnt(0)
	s_barrier
	s_andn2_b64 vcc, exec, s[8:9]
	s_cbranch_vccnz .LBB1_12
	v_add_u32_e32 v66, s24, v233
	ds_read_b128 v[50:53], v66 offset:96
	ds_read_b128 v[54:57], v66 offset:64
	ds_read_b128 v[58:61], v66 offset:32
	ds_read_b128 v[66:69], v66
	s_waitcnt lgkmcnt(3)
	v_pk_mul_f32 v[46:47], v[46:47], v[50:51]
	s_waitcnt lgkmcnt(2)
	v_pk_mul_f32 v[42:43], v[42:43], v[54:55]
	s_waitcnt lgkmcnt(1)
	v_pk_mul_f32 v[38:39], v[38:39], v[58:59]
	v_pk_mul_f32 v[48:49], v[48:49], v[52:53]
	v_pk_mul_f32 v[44:45], v[44:45], v[56:57]
	v_pk_mul_f32 v[40:41], v[40:41], v[60:61]
	s_waitcnt lgkmcnt(0)
	v_pk_mul_f32 v[36:37], v[36:37], v[68:69]
	v_pk_mul_f32 v[34:35], v[34:35], v[66:67]
	v_pk_mul_f32 v[30:31], v[30:31], v[50:51]
	v_pk_mul_f32 v[26:27], v[26:27], v[54:55]
	v_pk_mul_f32 v[22:23], v[22:23], v[58:59]
	v_pk_mul_f32 v[32:33], v[32:33], v[52:53]
	v_pk_mul_f32 v[28:29], v[28:29], v[56:57]
	v_pk_mul_f32 v[24:25], v[24:25], v[60:61]
	v_pk_mul_f32 v[20:21], v[20:21], v[68:69]
	v_pk_mul_f32 v[18:19], v[18:19], v[66:67]

.LBB1_13:
	s_add_i32 s16, s36, 0x2000
	s_cmpk_lg_i32 s36, 0x4000
	s_cselect_b32 s35, s16, 0
	s_waitcnt lgkmcnt(14)
	v_mfma_f32_32x32x16_f16 v[34:49], v[162:165], v[134:137], v[34:49]
	v_exp_f32_e32 v66, v66
	v_exp_f32_e32 v67, v67
	v_exp_f32_e32 v68, v68
	v_exp_f32_e32 v69, v69
	s_sub_i32 s43, s38, s27
	s_add_i32 s45, s43, 33
	s_add_i32 s43, s43, 35
	s_cmp_ge_i32 s18, s28
	s_cselect_b32 s44, s28, 0
	s_sub_i32 s44, s18, s44
	s_and_b64 s[48:49], s[6:7], exec
	s_cselect_b32 s43, s44, s43
	v_mad_i64_i32 v[252:253], s[50:51], s43, v244, v[222:223]
	s_add_i32 s44, s18, -2
	s_cmp_ge_i32 s44, s28
	s_cselect_b32 s46, s28, 0
	s_sub_i32 s44, s44, s46
	s_and_b64 s[48:49], s[6:7], exec
	s_cselect_b32 s44, s44, s45
	v_mad_i64_i32 v[254:255], s[50:51], s44, v244, v[224:225]
	s_add_i32 s52, s36, s30
	s_add_i32 s53, s35, s31
	s_add_i32 s46, s35, 0x2000
	s_cmpk_lg_i32 s35, 0x4000
	s_cselect_b32 s37, s46, 0
	s_add_i32 s39, s18, -2
	s_waitcnt lgkmcnt(12)
	v_mfma_f32_32x32x16_f16 v[18:33], v[162:165], v[142:145], v[18:33]
	v_exp_f32_e32 v70, v70
	v_exp_f32_e32 v71, v71
	v_exp_f32_e32 v72, v72
	v_exp_f32_e32 v73, v73
	v_add_u32_e32 v94, s35, v234
	ds_read_b128 v[206:209], v94
	ds_read_b128 v[202:205], v94 offset:4096
	s_waitcnt lgkmcnt(12)
	v_mfma_f32_32x32x16_f16 v[34:49], v[166:169], v[138:141], v[34:49]
	v_exp_f32_e32 v74, v74
	v_exp_f32_e32 v75, v75
	v_exp_f32_e32 v76, v76
	v_exp_f32_e32 v77, v77
	v_add_u32_e32 v94, s35, v235
	ds_read_b128 v[198:201], v94
	ds_read_b128 v[194:197], v94 offset:4096
	s_waitcnt lgkmcnt(12)
	v_mfma_f32_32x32x16_f16 v[18:33], v[166:169], v[102:105], v[18:33]
	v_exp_f32_e32 v78, v78
	v_exp_f32_e32 v79, v79
	v_exp_f32_e32 v80, v80
	v_exp_f32_e32 v81, v81
	v_add_u32_e32 v94, s35, v236
	ds_read_b128 v[190:193], v94
	ds_read_b128 v[186:189], v94 offset:4096
	s_waitcnt lgkmcnt(12)
	v_mfma_f32_32x32x16_f16 v[34:49], v[170:173], v[98:101], v[34:49]
	v_exp_f32_e32 v50, v50
	v_exp_f32_e32 v51, v51
	v_exp_f32_e32 v52, v52
	v_exp_f32_e32 v53, v53
	v_add_u32_e32 v94, s35, v237
	ds_read_b128 v[182:185], v94
	ds_read_b128 v[178:181], v94 offset:4096
	s_waitcnt lgkmcnt(12)
	v_mfma_f32_32x32x16_f16 v[18:33], v[170:173], v[82:85], v[18:33]
	v_exp_f32_e32 v54, v54
	v_exp_f32_e32 v55, v55
	v_exp_f32_e32 v56, v56
	v_exp_f32_e32 v57, v57
	s_waitcnt lgkmcnt(10)
	v_mfma_f32_32x32x16_f16 v[34:49], v[174:177], v[86:89], v[34:49]
	v_exp_f32_e32 v58, v58
	v_exp_f32_e32 v59, v59
	v_exp_f32_e32 v60, v60
	v_exp_f32_e32 v61, v61
	s_waitcnt lgkmcnt(8)
	v_mfma_f32_32x32x16_f16 v[18:33], v[174:177], v[90:93], v[18:33]
	v_exp_f32_e32 v62, v62
	v_exp_f32_e32 v63, v63
	v_exp_f32_e32 v64, v64
	v_exp_f32_e32 v65, v65
	s_mov_b32 m0, s52
	s_addk_i32 s52, 0x1000
	global_load_lds_dwordx4 v[252:253], off
	s_mov_b32 m0, s52
	v_lshl_add_u64 v[252:253], v[252:253], 0, s[10:11]
	global_load_lds_dwordx4 v[252:253], off
	s_mov_b32 m0, s53
	s_addk_i32 s53, 0x1000
	global_load_lds_dwordx4 v[254:255], off
	s_mov_b32 m0, s53
	v_lshl_add_u64 v[254:255], v[254:255], 0, s[10:11]
	global_load_lds_dwordx4 v[254:255], off
	s_waitcnt vmcnt(4) lgkmcnt(0)
	s_barrier
	s_andn2_b64 vcc, exec, s[8:9]
	s_cbranch_vccnz .LBB1_23
	v_add_u32_e32 v94, s24, v233
	ds_read_b128 v[82:85], v94 offset:96
	ds_read_b128 v[86:89], v94 offset:64
	ds_read_b128 v[90:93], v94
	ds_read_b128 v[94:97], v94 offset:32
	s_waitcnt lgkmcnt(3)
	v_pk_mul_f32 v[48:49], v[48:49], v[84:85]
	v_pk_mul_f32 v[46:47], v[46:47], v[82:83]
	s_waitcnt lgkmcnt(2)
	v_pk_mul_f32 v[44:45], v[44:45], v[88:89]
	v_pk_mul_f32 v[42:43], v[42:43], v[86:87]
	s_waitcnt lgkmcnt(0)
	v_pk_mul_f32 v[40:41], v[40:41], v[96:97]
	v_pk_mul_f32 v[38:39], v[38:39], v[94:95]
	v_pk_mul_f32 v[36:37], v[36:37], v[92:93]
	v_pk_mul_f32 v[34:35], v[34:35], v[90:91]
	v_pk_mul_f32 v[32:33], v[32:33], v[84:85]
	v_pk_mul_f32 v[30:31], v[30:31], v[82:83]
	v_pk_mul_f32 v[28:29], v[28:29], v[88:89]
	v_pk_mul_f32 v[26:27], v[26:27], v[86:87]
	v_pk_mul_f32 v[24:25], v[24:25], v[96:97]
	v_pk_mul_f32 v[22:23], v[22:23], v[94:95]
	v_pk_mul_f32 v[20:21], v[20:21], v[92:93]
	v_pk_mul_f32 v[18:19], v[18:19], v[90:91]
.LBB1_23:
	s_add_i32 s38, s38, 2
	s_add_i32 s18, s18, 2
	s_mov_b64 s[8:9], 0
	s_cmp_gt_i32 s38, 28
	s_cbranch_scc1 .LBB1_32
.LBB1_24:
	s_mov_b32 s5, s36
	s_mov_b32 s36, s37
	s_add_i32 s4, s33, s18
	s_mov_b64 s[8:9], -1
	s_cmp_eq_u32 s4, 4
	s_cbranch_scc0 .LBB1_5
	s_branch .LBB1_4

	.amdhsa_kernel _Z10attn64_fwdPKDF16_S0_S0_PDF16_
		.amdhsa_group_segment_fixed_size 0
		.amdhsa_private_segment_fixed_size 0
		.amdhsa_kernarg_size 32
		.amdhsa_user_sgpr_count 2
		.amdhsa_user_sgpr_dispatch_ptr 0
		.amdhsa_user_sgpr_queue_ptr 0
		.amdhsa_user_sgpr_kernarg_segment_ptr 1
		.amdhsa_user_sgpr_dispatch_id 0
		.amdhsa_user_sgpr_kernarg_preload_length 0
		.amdhsa_user_sgpr_kernarg_preload_offset 0
		.amdhsa_user_sgpr_private_segment_size 0
		.amdhsa_uses_dynamic_stack 0
		.amdhsa_enable_private_segment 0
		.amdhsa_system_sgpr_workgroup_id_x 1
		.amdhsa_system_sgpr_workgroup_id_y 0
		.amdhsa_system_sgpr_workgroup_id_z 0
		.amdhsa_system_sgpr_workgroup_info 0
		.amdhsa_system_vgpr_workitem_id 0
		.amdhsa_next_free_vgpr 256
		.amdhsa_next_free_sgpr 54
		.amdhsa_accum_offset 256
		.amdhsa_reserve_vcc 1
		.amdhsa_float_round_mode_32 0
		.amdhsa_float_round_mode_16_64 0
		.amdhsa_float_denorm_mode_32 3
		.amdhsa_float_denorm_mode_16_64 3
		.amdhsa_dx10_clamp 1
		.amdhsa_ieee_mode 1
		.amdhsa_fp16_overflow 0
		.amdhsa_tg_split 0
		.amdhsa_exception_fp_ieee_invalid_op 0
		.amdhsa_exception_fp_denorm_src 0
		.amdhsa_exception_fp_ieee_div_zero 0
		.amdhsa_exception_fp_ieee_overflow 0
		.amdhsa_exception_fp_ieee_underflow 0
		.amdhsa_exception_fp_ieee_inexact 0
		.amdhsa_exception_int_div_zero 0
	.end_amdhsa_kernel

amdhsa.kernels:
  - .agpr_count:     0
    .args:
      - .actual_access:  read_only
        .address_space:  global
        .offset:         0
        .size:           8
        .value_kind:     global_buffer
      - .actual_access:  read_only
        .address_space:  global
        .offset:         8
        .size:           8
        .value_kind:     global_buffer
      - .actual_access:  read_only
        .address_space:  global
        .offset:         16
        .size:           8
        .value_kind:     global_buffer
      - .actual_access:  read_only
        .address_space:  global
        .offset:         24
        .size:           8
        .value_kind:     global_buffer
      - .actual_access:  read_only
        .address_space:  global
        .offset:         32
        .size:           8
        .value_kind:     global_buffer
      - .address_space:  global
        .offset:         40
        .size:           8
        .value_kind:     global_buffer
      - .address_space:  global
        .offset:         48
        .size:           8
        .value_kind:     global_buffer
      - .address_space:  global
        .offset:         56
        .size:           8
        .value_kind:     global_buffer
      - .address_space:  global
        .offset:         64
        .size:           8
        .value_kind:     global_buffer
    .group_segment_fixed_size: 0
    .kernarg_segment_align: 8
    .kernarg_segment_size: 72
    .language:       OpenCL C
    .language_version:
      - 2
      - 0
    .max_flat_workgroup_size: 256
    .name:           _Z11prep_kernelPKfS0_S0_S0_S0_PDF16_S1_S1_P15HIP_vector_typeIfLj2EE
    .private_segment_fixed_size: 0
    .sgpr_count:     32
    .sgpr_spill_count: 0
    .symbol:         _Z11prep_kernelPKfS0_S0_S0_S0_PDF16_S1_S1_P15HIP_vector_typeIfLj2EE.kd
    .uniform_work_group_size: 1
    .uses_dynamic_stack: false
    .vgpr_count:     20
    .vgpr_spill_count: 0
    .wavefront_size: 64
  - .agpr_count:     0
    .args:
      - .address_space:  global
        .offset:         0
        .size:           8
        .value_kind:     global_buffer
      - .address_space:  global
        .offset:         8
        .size:           8
        .value_kind:     global_buffer
      - .address_space:  global
        .offset:         16
        .size:           8
        .value_kind:     global_buffer
      - .address_space:  global
        .offset:         24
        .size:           8
        .value_kind:     global_buffer
    .group_segment_fixed_size: 0
    .kernarg_segment_align: 8
    .kernarg_segment_size: 32
    .language:       OpenCL C
    .language_version:
      - 2
      - 0
    .max_flat_workgroup_size: 512
    .name:           _Z10attn64_fwdPKDF16_S0_S0_PDF16_
    .private_segment_fixed_size: 0
    .sgpr_count:     60
    .sgpr_spill_count: 0
    .symbol:         _Z10attn64_fwdPKDF16_S0_S0_PDF16_.kd
    .uniform_work_group_size: 1
    .uses_dynamic_stack: false
    .vgpr_count:     256
    .vgpr_spill_count: 0
    .wavefront_size: 64
  - .agpr_count:     0
    .args:
      - .address_space:  global
        .offset:         0
        .size:           8
        .value_kind:     global_buffer
      - .address_space:  global
        .offset:         8
        .size:           8
        .value_kind:     global_buffer
      - .address_space:  global
        .offset:         16
        .size:           8
        .value_kind:     global_buffer
      - .address_space:  global
        .offset:         24
        .size:           8
        .value_kind:     global_buffer
      - .address_space:  global
        .offset:         32
        .size:           8
        .value_kind:     global_buffer
      - .address_space:  global
        .offset:         40
        .size:           8
        .value_kind:     global_buffer
      - .actual_access:  read_only
        .address_space:  global
        .offset:         48
        .size:           8
        .value_kind:     global_buffer
      - .offset:         56
        .size:           4
        .value_kind:     by_value
      - .offset:         60
        .size:           4
        .value_kind:     by_value
      - .offset:         64
        .size:           4
        .value_kind:     by_value
    .group_segment_fixed_size: 32768
    .kernarg_segment_align: 8
    .kernarg_segment_size: 68
    .language:       OpenCL C
    .language_version:
      - 2
      - 0
    .max_flat_workgroup_size: 768
    .name:           _Z7gemm_dbILi256ELi192ELi64ELi96ELi64ELi2ELi1ELi4EEvPKDF16_S1_PfPDF16_S3_S3_PK15HIP_vector_typeIfLj2EEiii
    .private_segment_fixed_size: 0
    .sgpr_count:     27
    .sgpr_spill_count: 0
    .symbol:         _Z7gemm_dbILi256ELi192ELi64ELi96ELi64ELi2ELi1ELi4EEvPKDF16_S1_PfPDF16_S3_S3_PK15HIP_vector_typeIfLj2EEiii.kd
    .uniform_work_group_size: 1
    .uses_dynamic_stack: false
    .vgpr_count:     141
    .vgpr_spill_count: 0
    .wavefront_size: 64
  - .agpr_count:     0
    .args:
      - .address_space:  global
        .offset:         0
        .size:           8
        .value_kind:     global_buffer
      - .address_space:  global
        .offset:         8
        .size:           8
        .value_kind:     global_buffer
      - .address_space:  global
        .offset:         16
        .size:           8
        .value_kind:     global_buffer
      - .address_space:  global
        .offset:         24
        .size:           8
        .value_kind:     global_buffer
      - .address_space:  global
        .offset:         32
        .size:           8
        .value_kind:     global_buffer
      - .address_space:  global
        .offset:         40
        .size:           8
        .value_kind:     global_buffer
      - .actual_access:  read_only
        .address_space:  global
        .offset:         48
        .size:           8
        .value_kind:     global_buffer
      - .offset:         56
        .size:           4
        .value_kind:     by_value
      - .offset:         60
        .size:           4
        .value_kind:     by_value
      - .offset:         64
        .size:           4
        .value_kind:     by_value
    .group_segment_fixed_size: 0
    .kernarg_segment_align: 8
    .kernarg_segment_size: 68
    .language:       OpenCL C
    .language_version:
      - 2
      - 0
    .max_flat_workgroup_size: 512
    .name:           _Z7gemm_dbILi128ELi128ELi64ELi64ELi64ELi3ELi0ELi4EEvPKDF16_S1_PfPDF16_S3_S3_PK15HIP_vector_typeIfLj2EEiii
    .private_segment_fixed_size: 0
    .sgpr_count:     26
    .sgpr_spill_count: 0
    .symbol:         _Z7gemm_dbILi128ELi128ELi64ELi64ELi64ELi3ELi0ELi4EEvPKDF16_S1_PfPDF16_S3_S3_PK15HIP_vector_typeIfLj2EEiii.kd
    .uniform_work_group_size: 1
    .uses_dynamic_stack: false
    .vgpr_count:     168
    .vgpr_spill_count: 0
    .wavefront_size: 64
